# plus proj K-loop LDS-DMA loads in SGPR-base form (no 64-bit address arithmetic per load)
# baseline (speedup 1.0000x reference)
.LBB0_235:
	s_add_u32 s4, s0, 0xfffe0080
	s_addc_u32 s5, s1, -1
	s_add_i32 s52, 0, 0x10000
	s_cmp_eq_u32 s51, 4
	s_cselect_b32 s7, s21, s5
	s_cselect_b32 s6, s29, s4
	s_cselect_b32 s5, s23, s50
	s_cselect_b32 s4, s48, s49
	s_add_i32 s53, 0, 0x14000
	ds_read_b128 v[20:23], v192
	ds_read_b128 v[24:27], v249
	ds_read_b128 v[28:31], v192 offset:2048
	ds_read_b128 v[32:35], v249 offset:2048
	ds_read_b128 v[4:7], v192 offset:16384
	ds_read_b128 v[8:11], v249 offset:16384
	ds_read_b128 v[12:15], v192 offset:18432
	ds_read_b128 v[16:19], v249 offset:18432
	s_add_i32 m0, s37, 0xc000
	ds_read_b128 v[184:187], v193
	ds_read_b128 v[188:191], v250
	ds_read_b128 v[194:197], v193 offset:2048
	ds_read_b128 v[198:201], v250 offset:2048
	ds_read_b128 v[202:205], v193 offset:4096
	ds_read_b128 v[206:209], v250 offset:4096
	ds_read_b128 v[226:229], v193 offset:6144
	ds_read_b128 v[230:233], v250 offset:6144
	global_load_lds_dwordx4 v180, s[0:1]
	s_add_i32 m0, s37, 0xe000
	s_nop 0
	global_load_lds_dwordx4 v182, s[0:1]
	s_waitcnt vmcnt(8)
	s_waitcnt lgkmcnt(0)
	s_barrier
	s_setprio 1
	v_mfma_f32_16x16x128_f8f6f4 v[96:99], v[20:27], v[184:191], v[96:99]
	v_mfma_f32_16x16x128_f8f6f4 v[92:95], v[28:35], v[184:191], v[92:95]
	v_mfma_f32_16x16x128_f8f6f4 v[88:91], v[20:27], v[194:201], v[88:91]
	v_mfma_f32_16x16x128_f8f6f4 v[84:87], v[28:35], v[194:201], v[84:87]
	v_mfma_f32_16x16x128_f8f6f4 v[80:83], v[20:27], v[202:209], v[80:83]
	v_mfma_f32_16x16x128_f8f6f4 v[76:79], v[28:35], v[202:209], v[76:79]
	v_mfma_f32_16x16x128_f8f6f4 v[72:75], v[20:27], v[226:233], v[72:75]
	v_mfma_f32_16x16x128_f8f6f4 v[68:71], v[28:35], v[226:233], v[68:71]
	v_mfma_f32_16x16x128_f8f6f4 v[160:163], v[4:11], v[184:191], v[160:163]
	v_mfma_f32_16x16x128_f8f6f4 v[156:159], v[12:19], v[184:191], v[156:159]
	v_mfma_f32_16x16x128_f8f6f4 v[152:155], v[4:11], v[194:201], v[152:155]
	v_mfma_f32_16x16x128_f8f6f4 v[148:151], v[12:19], v[194:201], v[148:151]
	v_mfma_f32_16x16x128_f8f6f4 v[144:147], v[4:11], v[202:209], v[144:147]
	v_mfma_f32_16x16x128_f8f6f4 v[140:143], v[12:19], v[202:209], v[140:143]
	v_mfma_f32_16x16x128_f8f6f4 v[136:139], v[4:11], v[226:233], v[136:139]
	v_mfma_f32_16x16x128_f8f6f4 v[132:135], v[12:19], v[226:233], v[132:135]
	s_setprio 0
	s_barrier
	s_add_i32 s52, s52, s36
	s_mov_b32 m0, s52
	ds_read_b128 v[194:197], v193 offset:16384
	ds_read_b128 v[198:201], v250 offset:16384
	ds_read_b128 v[202:205], v193 offset:18432
	ds_read_b128 v[206:209], v250 offset:18432
	ds_read_b128 v[226:229], v193 offset:20480
	ds_read_b128 v[230:233], v250 offset:20480
	ds_read_b128 v[234:237], v193 offset:22528
	ds_read_b128 v[238:241], v250 offset:22528
	global_load_lds_dwordx4 v176, s[4:5]
	s_add_i32 m0, s52, 0x2000
	s_add_u32 s54, s4, 0x20000
	s_addc_u32 s55, s5, 0
	s_add_i32 s52, s53, s36
	global_load_lds_dwordx4 v172, s[4:5]
	s_mov_b32 m0, s52
	s_nop 0
	global_load_lds_dwordx4 v176, s[54:55]
	s_add_i32 m0, s52, 0x2000
	s_nop 0
	global_load_lds_dwordx4 v172, s[54:55]
	s_mov_b32 m0, s37
	s_nop 0
	global_load_lds_dwordx4 v178, s[6:7]
	s_mov_b32 m0, s38
	s_nop 0
	global_load_lds_dwordx4 v174, s[6:7]
	s_waitcnt vmcnt(8)
	s_waitcnt lgkmcnt(0)
	s_barrier
	s_setprio 1
	v_mfma_f32_16x16x128_f8f6f4 v[64:67], v[20:27], v[194:201], v[64:67]
	v_mfma_f32_16x16x128_f8f6f4 v[60:63], v[28:35], v[194:201], v[60:63]
	v_mfma_f32_16x16x128_f8f6f4 v[56:59], v[20:27], v[202:209], v[56:59]
	v_mfma_f32_16x16x128_f8f6f4 v[52:55], v[28:35], v[202:209], v[52:55]
	v_mfma_f32_16x16x128_f8f6f4 v[48:51], v[20:27], v[226:233], v[48:51]
	v_mfma_f32_16x16x128_f8f6f4 v[44:47], v[28:35], v[226:233], v[44:47]
	v_mfma_f32_16x16x128_f8f6f4 v[40:43], v[20:27], v[234:241], v[40:43]
	v_mfma_f32_16x16x128_f8f6f4 v[36:39], v[28:35], v[234:241], v[36:39]
	v_mfma_f32_16x16x128_f8f6f4 v[128:131], v[4:11], v[194:201], v[128:131]
	v_mfma_f32_16x16x128_f8f6f4 v[124:127], v[12:19], v[194:201], v[124:127]
	v_mfma_f32_16x16x128_f8f6f4 v[120:123], v[4:11], v[202:209], v[120:123]
	v_mfma_f32_16x16x128_f8f6f4 v[116:119], v[12:19], v[202:209], v[116:119]
	v_mfma_f32_16x16x128_f8f6f4 v[112:115], v[4:11], v[226:233], v[112:115]
	v_mfma_f32_16x16x128_f8f6f4 v[108:111], v[12:19], v[226:233], v[108:111]
	v_mfma_f32_16x16x128_f8f6f4 v[104:107], v[4:11], v[234:241], v[104:107]
	v_mfma_f32_16x16x128_f8f6f4 v[100:103], v[12:19], v[234:241], v[100:103]
	s_setprio 0
	s_barrier
	s_add_i32 s52, 0, 0x18000
	s_add_i32 s53, 0, 0x1c000
	ds_read_b128 v[4:7], v192 offset:32768
	ds_read_b128 v[8:11], v249 offset:32768
	ds_read_b128 v[12:15], v192 offset:34816
	ds_read_b128 v[16:19], v249 offset:34816
	ds_read_b128 v[20:23], v192 offset:49152
	ds_read_b128 v[24:27], v249 offset:49152
	ds_read_b128 v[28:31], v192 offset:51200
	ds_read_b128 v[32:35], v249 offset:51200
	s_add_u32 s6, s6, 0x20000
	s_addc_u32 s7, s7, 0
	s_mov_b32 m0, s39
	ds_read_b128 v[194:197], v193 offset:32768
	ds_read_b128 v[198:201], v250 offset:32768
	ds_read_b128 v[202:205], v193 offset:34816
	ds_read_b128 v[206:209], v250 offset:34816
	ds_read_b128 v[226:229], v193 offset:36864
	ds_read_b128 v[230:233], v250 offset:36864
	ds_read_b128 v[234:237], v193 offset:38912
	ds_read_b128 v[238:241], v250 offset:38912
	global_load_lds_dwordx4 v178, s[6:7]
	s_mov_b32 m0, s42
	s_nop 0
	global_load_lds_dwordx4 v174, s[6:7]
	s_waitcnt vmcnt(8)
	s_waitcnt lgkmcnt(0)
	s_barrier
	s_setprio 1
	v_mfma_f32_16x16x128_f8f6f4 v[96:99], v[4:11], v[194:201], v[96:99]
	v_mfma_f32_16x16x128_f8f6f4 v[92:95], v[12:19], v[194:201], v[92:95]
	v_mfma_f32_16x16x128_f8f6f4 v[88:91], v[4:11], v[202:209], v[88:91]
	v_mfma_f32_16x16x128_f8f6f4 v[84:87], v[12:19], v[202:209], v[84:87]
	v_mfma_f32_16x16x128_f8f6f4 v[80:83], v[4:11], v[226:233], v[80:83]
	v_mfma_f32_16x16x128_f8f6f4 v[76:79], v[12:19], v[226:233], v[76:79]
	v_mfma_f32_16x16x128_f8f6f4 v[72:75], v[4:11], v[234:241], v[72:75]
	v_mfma_f32_16x16x128_f8f6f4 v[68:71], v[12:19], v[234:241], v[68:71]
	v_mfma_f32_16x16x128_f8f6f4 v[160:163], v[20:27], v[194:201], v[160:163]
	v_mfma_f32_16x16x128_f8f6f4 v[156:159], v[28:35], v[194:201], v[156:159]
	v_mfma_f32_16x16x128_f8f6f4 v[152:155], v[20:27], v[202:209], v[152:155]
	v_mfma_f32_16x16x128_f8f6f4 v[148:151], v[28:35], v[202:209], v[148:151]
	v_mfma_f32_16x16x128_f8f6f4 v[144:147], v[20:27], v[226:233], v[144:147]
	v_mfma_f32_16x16x128_f8f6f4 v[140:143], v[28:35], v[226:233], v[140:143]
	v_mfma_f32_16x16x128_f8f6f4 v[136:139], v[20:27], v[234:241], v[136:139]
	v_mfma_f32_16x16x128_f8f6f4 v[132:135], v[28:35], v[234:241], v[132:135]
	s_setprio 0
	s_barrier
	s_add_u32 s58, s4, 0x80
	s_addc_u32 s59, s5, 0
	s_add_u32 s62, s6, 0xfffe0080
	s_addc_u32 s63, s7, -1
	s_add_i32 s6, s52, s36
	s_mov_b32 m0, s6
	ds_read_b128 v[194:197], v193 offset:49152
	ds_read_b128 v[198:201], v250 offset:49152
	ds_read_b128 v[202:205], v193 offset:51200
	ds_read_b128 v[206:209], v250 offset:51200
	ds_read_b128 v[226:229], v193 offset:53248
	ds_read_b128 v[230:233], v250 offset:53248
	ds_read_b128 v[234:237], v193 offset:55296
	ds_read_b128 v[238:241], v250 offset:55296
	global_load_lds_dwordx4 v176, s[58:59]
	s_add_i32 m0, s6, 0x2000
	s_add_u32 s4, s4, 0x20080
	s_addc_u32 s5, s5, 0
	s_add_i32 s6, s53, s36
	global_load_lds_dwordx4 v172, s[58:59]
	s_mov_b32 m0, s6
	s_nop 0
	global_load_lds_dwordx4 v176, s[4:5]
	s_add_i32 m0, s6, 0x2000
	s_nop 0
	global_load_lds_dwordx4 v172, s[4:5]
	s_mov_b32 m0, s45
	s_nop 0
	global_load_lds_dwordx4 v178, s[62:63]
	s_mov_b32 m0, s46
	s_nop 0
	global_load_lds_dwordx4 v174, s[62:63]
	s_waitcnt vmcnt(8)
	s_waitcnt lgkmcnt(0)
	s_barrier
	s_setprio 1
	v_mfma_f32_16x16x128_f8f6f4 v[64:67], v[4:11], v[194:201], v[64:67]
	v_mfma_f32_16x16x128_f8f6f4 v[60:63], v[12:19], v[194:201], v[60:63]
	v_mfma_f32_16x16x128_f8f6f4 v[56:59], v[4:11], v[202:209], v[56:59]
	v_mfma_f32_16x16x128_f8f6f4 v[52:55], v[12:19], v[202:209], v[52:55]
	v_mfma_f32_16x16x128_f8f6f4 v[48:51], v[4:11], v[226:233], v[48:51]
	v_mfma_f32_16x16x128_f8f6f4 v[44:47], v[12:19], v[226:233], v[44:47]
	v_mfma_f32_16x16x128_f8f6f4 v[40:43], v[4:11], v[234:241], v[40:43]
	v_mfma_f32_16x16x128_f8f6f4 v[36:39], v[12:19], v[234:241], v[36:39]
	v_mfma_f32_16x16x128_f8f6f4 v[128:131], v[20:27], v[194:201], v[128:131]
	v_mfma_f32_16x16x128_f8f6f4 v[124:127], v[28:35], v[194:201], v[124:127]
	v_mfma_f32_16x16x128_f8f6f4 v[120:123], v[20:27], v[202:209], v[120:123]
	v_mfma_f32_16x16x128_f8f6f4 v[116:119], v[28:35], v[202:209], v[116:119]
	v_mfma_f32_16x16x128_f8f6f4 v[112:115], v[20:27], v[226:233], v[112:115]
	v_mfma_f32_16x16x128_f8f6f4 v[108:111], v[28:35], v[226:233], v[108:111]
	v_mfma_f32_16x16x128_f8f6f4 v[104:107], v[20:27], v[234:241], v[104:107]
	v_mfma_f32_16x16x128_f8f6f4 v[100:103], v[28:35], v[234:241], v[100:103]
	s_setprio 0
	s_barrier
	s_add_i32 s51, s51, 2
	s_add_u32 s0, s0, 0x100
	s_addc_u32 s1, s1, 0
	s_add_u32 s49, s49, 0x100
	s_addc_u32 s50, s50, 0
	s_cmp_gt_u32 s51, 5
	s_cbranch_scc0 .LBB0_235
	s_and_b64 vcc, exec, s[18:19]
	s_cbranch_vccz .LBB0_238
	s_barrier
